# prologue weight conversion: expert gate/up items software-pipelined (next tile's 16 loads issued before the current tile's transpose/convert/store)
# baseline (speedup 1.0000x reference)
; __device__ __forceinline__ void p0_prologue(Frame& F) {
;     ...
;     for (int it = gw; it < NITEMS; it += NGW) {
;         int r = it;
.Lpp_egu_chk:
	s_add_i32 s97, s3, s8
	s_cmp_gt_u32 s97, 0x9bff
	s_cbranch_scc1 .Lpp_egu_tail
	s_mov_b32 s3, s97
	s_mov_b32 s99, s74
	s_mov_b64 s[100:101], s[0:1]
	s_bfe_u32 s6, s3, 0x30004
	s_lshl_b32 s75, s6, 6
	s_cmp_gt_u32 s6, 3
	s_mov_b64 s[0:1], -1
	s_cbranch_scc0 .Lpp_egu_a38
	s_lshl_b32 s0, s6, 7
	s_and_b32 s1, s75, 64
	s_or_b32 s0, s0, s1
	s_bitset1_b32 s0, 7
	s_add_i32 s74, s0, 0xfffffe00
	s_mov_b64 s[0:1], 0

; #define GAS __attribute__((address_space(1)))
; #define LAS __attribute__((address_space(3)))
; #define LDS_WAIT() asm volatile("s_waitcnt lgkmcnt(0)" ::: "memory")
; __device__ __forceinline__ void p0_transpose_item64_f8(const float* W, int K, int N, unsigned char* WT, int dst_n0, LAS float* scr, int kb, int nb, int lane, const float wsc) {
;     const int k0 = 64 * kb, n0 = 64 * nb; const int r = lane >> 4, c4 = lane & 15;
;     f32x4 v[16];
; #pragma unroll
;     for (int i = 0; i < 16; ++i) v[i] = __builtin_nontemporal_load((const GAS f32x4*)(W + (size_t)(k0 + 4 * i + r) * N + n0 + 4 * c4));
; #pragma unroll
;     for (int i = 0; i < 16; ++i) { const int k = 4 * i + r; *(LAS f32x4*)(scr + k * 64 + 4 * (c4 ^ (k >> 3))) = v[i]; }
;     LDS_WAIT(); asm volatile("" ::: "memory");
;     const int c = lane & 3;
; #pragma unroll
;     for (int j = 0; j < 4; ++j) { const int n = (lane >> 2) + 16 * j;
;         unsigned o[4];
; #pragma unroll
;         for (int d = 0; d < 4; ++d) { float f[4];
; #pragma unroll
;             for (int e = 0; e < 4; ++e) { const int k = 16 * c + 4 * d + e; f[e] = scr[k * 64 + 4 * ((n >> 2) ^ (k >> 3)) + (n & 3)] * wsc; }
;             int p = __builtin_amdgcn_cvt_pk_fp8_f32(f[0], f[1], 0, false); p = __builtin_amdgcn_cvt_pk_fp8_f32(f[2], f[3], p, true); o[d] = (unsigned)p; }
;         u32x4 ov; ov.x = o[0]; ov.y = o[1]; ov.z = o[2]; ov.w = o[3];
;         *(GAS u32x4*)(WT + (size_t)(dst_n0 + n) * K + k0 + 16 * c) = ov; }
.Lpp_egu_a40:
	v_mov_b32_e32 v4, s55
	ds_read_b64 v[18:19], v4
	s_add_i32 s0, s3, 0xffffe400
	s_lshr_b32 s6, s0, 7
	s_lshl_b64 s[0:1], s[6:7], 19
	s_lshl_b64 s[76:77], s[6:7], 21
	s_waitcnt lgkmcnt(0)
	v_readfirstlane_b32 s79, v18
	v_readfirstlane_b32 s78, v19
	s_add_u32 s6, s79, s76
	s_addc_u32 s76, s78, s77
	s_add_u32 s77, s11, s0
	s_addc_u32 s78, s12, s1
	s_lshl_b32 s0, s3, 6
	s_and_b32 s79, s0, 0x3c0
	s_lshl_b32 s0, s75, 2
	s_add_u32 s0, s6, s0
	v_or_b32_e32 v11, s79, v3
	s_addc_u32 s1, s76, 0
	v_lshlrev_b32_e32 v4, 2, v2
	v_lshl_add_u64 v[18:19], s[0:1], 0, v[4:5]
	v_lshlrev_b32_e32 v4, 11, v11
	v_lshl_add_u64 v[122:123], v[18:19], 0, v[4:5]
	v_add_co_u32_e32 v70, vcc, s56, v122
	v_add_u32_e32 v4, v9, v17
	s_nop 0
	v_addc_co_u32_e32 v71, vcc, 0, v123, vcc
	v_add_co_u32_e32 v74, vcc, s39, v122
	global_load_dwordx4 v[18:21], v[122:123], off nt
	s_nop 0
	global_load_dwordx4 v[70:73], v[70:71], off nt
	v_addc_co_u32_e32 v75, vcc, 0, v123, vcc
	v_add_co_u32_e32 v78, vcc, s57, v122
	s_add_u32 s0, s77, s79
	s_nop 0
	v_addc_co_u32_e32 v79, vcc, 0, v123, vcc
	v_add_co_u32_e32 v82, vcc, s40, v122
	global_load_dwordx4 v[74:77], v[74:75], off nt
	s_nop 0
	global_load_dwordx4 v[78:81], v[78:79], off nt
	v_addc_co_u32_e32 v83, vcc, 0, v123, vcc
	v_add_co_u32_e32 v86, vcc, s58, v122
	s_addc_u32 s1, s78, 0
	s_nop 0
	v_addc_co_u32_e32 v87, vcc, 0, v123, vcc
	v_add_co_u32_e32 v90, vcc, s41, v122
	global_load_dwordx4 v[82:85], v[82:83], off nt
	s_nop 0
	global_load_dwordx4 v[86:89], v[86:87], off nt
	v_addc_co_u32_e32 v91, vcc, 0, v123, vcc
	v_add_co_u32_e32 v94, vcc, s59, v122
	s_nop 1
	v_addc_co_u32_e32 v95, vcc, 0, v123, vcc
	v_add_co_u32_e32 v98, vcc, s42, v122
	global_load_dwordx4 v[90:93], v[90:91], off nt
	s_nop 0
	global_load_dwordx4 v[94:97], v[94:95], off nt
	v_addc_co_u32_e32 v99, vcc, 0, v123, vcc
	v_add_co_u32_e32 v102, vcc, s60, v122
	s_nop 1
	v_addc_co_u32_e32 v103, vcc, 0, v123, vcc
	v_add_co_u32_e32 v106, vcc, s43, v122
	global_load_dwordx4 v[98:101], v[98:99], off nt
	s_nop 0
	global_load_dwordx4 v[102:105], v[102:103], off nt
	v_addc_co_u32_e32 v107, vcc, 0, v123, vcc
	v_add_co_u32_e32 v110, vcc, s61, v122
	s_nop 1
	v_addc_co_u32_e32 v111, vcc, 0, v123, vcc
	v_add_co_u32_e32 v114, vcc, s44, v122
	global_load_dwordx4 v[106:109], v[106:107], off nt
	s_nop 0
	global_load_dwordx4 v[110:113], v[110:111], off nt
	v_addc_co_u32_e32 v115, vcc, 0, v123, vcc
	v_add_co_u32_e32 v118, vcc, s62, v122
	s_nop 1
	v_addc_co_u32_e32 v119, vcc, 0, v123, vcc
	v_add_co_u32_e32 v124, vcc, s45, v122
	global_load_dwordx4 v[114:117], v[114:115], off nt
	s_nop 0
	global_load_dwordx4 v[118:121], v[118:119], off nt
	v_addc_co_u32_e32 v125, vcc, 0, v123, vcc
	v_add_co_u32_e32 v126, vcc, s63, v122
	s_nop 1
	v_addc_co_u32_e32 v127, vcc, 0, v123, vcc
	global_load_dwordx4 v[122:125], v[124:125], off nt
	s_nop 0
	global_load_dwordx4 v[126:129], v[126:127], off nt
	v_add_u32_e32 v4, v30, v65
	ds_read2st64_b32 v[190:191], v4 offset1:1
	ds_read2st64_b32 v[192:193], v4 offset0:2 offset1:3
	ds_read2st64_b32 v[196:197], v4 offset0:4 offset1:5
	ds_read2st64_b32 v[198:199], v4 offset0:6 offset1:7
	v_mov_b32_e32 v194, v5
	v_mov_b32_e32 v195, v5
	s_waitcnt lgkmcnt(3)
	v_mul_f32_e32 v4, 0x43800000, v190
	v_mul_f32_e32 v11, 0x43800000, v191
	v_cvt_pk_fp8_f32 v194, v4, v11
	s_waitcnt lgkmcnt(2)
	v_mul_f32_e32 v4, 0x43800000, v192
	v_mul_f32_e32 v11, 0x43800000, v193
	s_waitcnt lgkmcnt(0)
	v_mul_f32_e32 v13, 0x43800000, v198
	v_cvt_pk_fp8_f32 v194, v4, v11 op_sel:[0,0,1]
	v_mul_f32_e32 v4, 0x43800000, v196
	v_mul_f32_e32 v11, 0x43800000, v197
	v_cvt_pk_fp8_f32 v195, v4, v11
	v_mul_f32_e32 v11, 0x43800000, v199
	v_add_u32_e32 v4, v31, v32
	ds_read_b32 v4, v4
	v_cvt_pk_fp8_f32 v195, v13, v11 op_sel:[0,0,1]
	v_add_u32_e32 v11, v31, v65
	ds_read2st64_b32 v[192:193], v11 offset0:9 offset1:10
	v_add_u32_e32 v13, v33, v29
	ds_read_b32 v11, v11 offset:2816
	ds_read_b32 v13, v13
	v_add_u32_e32 v197, v33, v65
	s_waitcnt lgkmcnt(2)
	v_mul_f32_e32 v15, 0x43800000, v192
	v_mul_f32_e32 v69, 0x43800000, v193
	ds_read2st64_b32 v[192:193], v197 offset0:13 offset1:14
	v_mul_f32_e32 v4, 0x43800000, v4
	v_mov_b32_e32 v196, v5
	v_cvt_pk_fp8_f32 v196, v4, v15
	s_waitcnt lgkmcnt(1)
	v_mul_f32_e32 v4, 0x43800000, v13
	ds_read_b32 v13, v197 offset:3840
	s_waitcnt lgkmcnt(1)
	v_mul_f32_e32 v15, 0x43800000, v192
	v_mov_b32_e32 v197, v5
	v_cvt_pk_fp8_f32 v197, v4, v15
	v_mul_f32_e32 v11, 0x43800000, v11
	v_cvt_pk_fp8_f32 v196, v69, v11 op_sel:[0,0,1]
	v_mul_f32_e32 v4, 0x43800000, v193
	s_waitcnt lgkmcnt(0)
	v_mul_f32_e32 v11, 0x43800000, v13
	v_cvt_pk_fp8_f32 v197, v4, v11 op_sel:[0,0,1]
	v_add_u32_e32 v4, s99, v28
	v_lshlrev_b64 v[192:193], 10, v[4:5]
	v_add_u32_e32 v4, v35, v65
	ds_read2st64_b32 v[198:199], v4 offset1:1
	ds_read2st64_b32 v[200:201], v4 offset0:2 offset1:3
	ds_read2st64_b32 v[202:203], v4 offset0:4 offset1:5
	ds_read2st64_b32 v[204:205], v4 offset0:6 offset1:7
	v_lshl_add_u64 v[190:191], s[100:101], 0, v[6:7]
	v_lshl_add_u64 v[192:193], v[190:191], 0, v[192:193]
	global_store_dwordx4 v[192:193], v[194:197], off
	s_waitcnt lgkmcnt(3)
	v_mul_f32_e32 v4, 0x43800000, v198
	v_mul_f32_e32 v11, 0x43800000, v199
	v_mov_b32_e32 v198, v5
	v_cvt_pk_fp8_f32 v198, v4, v11
	s_waitcnt lgkmcnt(2)
	v_mul_f32_e32 v4, 0x43800000, v200
	v_mul_f32_e32 v11, 0x43800000, v201
	v_mov_b32_e32 v199, v5
	v_cvt_pk_fp8_f32 v198, v4, v11 op_sel:[0,0,1]
	s_waitcnt lgkmcnt(1)
	v_mul_f32_e32 v4, 0x43800000, v202
	v_mul_f32_e32 v11, 0x43800000, v203
	v_cvt_pk_fp8_f32 v199, v4, v11
	s_waitcnt lgkmcnt(0)
; #define GAS __attribute__((address_space(1)))
; #define LAS __attribute__((address_space(3)))
; #define LDS_WAIT() asm volatile("s_waitcnt lgkmcnt(0)" ::: "memory")
; __device__ __forceinline__ void p0_transpose_item64_f8(const float* W, int K, int N, unsigned char* WT, int dst_n0, LAS float* scr, int kb, int nb, int lane, const float wsc) {
;     ...
;     for (int i = 0; i < 16; ++i) { const int k = 4 * i + r; *(LAS f32x4*)(scr + k * 64 + 4 * (c4 ^ (k >> 3))) = v[i]; }
;     ...
;     const int c = lane & 3;
; #pragma unroll
;     for (int j = 0; j < 4; ++j) { const int n = (lane >> 2) + 16 * j;
;         unsigned o[4];
; #pragma unroll
;         for (int d = 0; d < 4; ++d) { float f[4];
; #pragma unroll
;             for (int e = 0; e < 4; ++e) { const int k = 16 * c + 4 * d + e; f[e] = scr[k * 64 + 4 * ((n >> 2) ^ (k >> 3)) + (n & 3)] * wsc; }
;             int p = __builtin_amdgcn_cvt_pk_fp8_f32(f[0], f[1], 0, false); p = __builtin_amdgcn_cvt_pk_fp8_f32(f[2], f[3], p, true); o[d] = (unsigned)p; }
;         u32x4 ov; ov.x = o[0]; ov.y = o[1]; ov.z = o[2]; ov.w = o[3];
;         *(GAS u32x4*)(WT + (size_t)(dst_n0 + n) * K + k0 + 16 * c) = ov; }
;     LDS_WAIT(); asm volatile("" ::: "memory");
	v_mul_f32_e32 v13, 0x43800000, v204
	v_mul_f32_e32 v11, 0x43800000, v205
	v_add_u32_e32 v4, v36, v32
	v_cvt_pk_fp8_f32 v199, v13, v11 op_sel:[0,0,1]
	v_add_u32_e32 v11, v36, v65
	ds_read2st64_b32 v[192:193], v11 offset0:9 offset1:10
	ds_read_b32 v4, v4
	v_add_u32_e32 v13, v37, v29
	ds_read_b32 v11, v11 offset:2816
	ds_read_b32 v13, v13
	v_add_u32_e32 v194, v37, v65
	s_waitcnt lgkmcnt(3)
	v_mul_f32_e32 v15, 0x43800000, v192
	v_mul_f32_e32 v69, 0x43800000, v193
	ds_read2st64_b32 v[192:193], v194 offset0:13 offset1:14
	s_waitcnt lgkmcnt(3)
	v_mul_f32_e32 v4, 0x43800000, v4
	v_mov_b32_e32 v200, v5
	v_cvt_pk_fp8_f32 v200, v4, v15
	s_waitcnt lgkmcnt(1)
	v_mul_f32_e32 v4, 0x43800000, v13
	ds_read_b32 v13, v194 offset:3840
	s_waitcnt lgkmcnt(1)
	v_mul_f32_e32 v15, 0x43800000, v192
	v_mov_b32_e32 v201, v5
	v_cvt_pk_fp8_f32 v201, v4, v15
	v_mul_f32_e32 v11, 0x43800000, v11
	v_cvt_pk_fp8_f32 v200, v69, v11 op_sel:[0,0,1]
	v_mul_f32_e32 v4, 0x43800000, v193
	s_waitcnt lgkmcnt(0)
	v_mul_f32_e32 v11, 0x43800000, v13
	v_cvt_pk_fp8_f32 v201, v4, v11 op_sel:[0,0,1]
	v_add_u32_e32 v4, s99, v34
	v_lshlrev_b64 v[192:193], 10, v[4:5]
	v_add_u32_e32 v4, v39, v65
	ds_read2st64_b32 v[194:195], v4 offset1:1
	ds_read2st64_b32 v[196:197], v4 offset0:2 offset1:3
	ds_read2st64_b32 v[202:203], v4 offset0:4 offset1:5
	ds_read2st64_b32 v[204:205], v4 offset0:6 offset1:7
	v_lshl_add_u64 v[192:193], v[190:191], 0, v[192:193]
	global_store_dwordx4 v[192:193], v[198:201], off
	s_waitcnt lgkmcnt(3)
	v_mul_f32_e32 v4, 0x43800000, v194
	v_mul_f32_e32 v11, 0x43800000, v195
	v_mov_b32_e32 v194, v5
	v_cvt_pk_fp8_f32 v194, v4, v11
	s_waitcnt lgkmcnt(2)
	v_mul_f32_e32 v4, 0x43800000, v196
	v_mul_f32_e32 v11, 0x43800000, v197
	v_mov_b32_e32 v195, v5
	v_cvt_pk_fp8_f32 v194, v4, v11 op_sel:[0,0,1]
	s_waitcnt lgkmcnt(1)
	v_mul_f32_e32 v4, 0x43800000, v202
	v_mul_f32_e32 v11, 0x43800000, v203
	v_cvt_pk_fp8_f32 v195, v4, v11
	s_waitcnt lgkmcnt(0)
	v_mul_f32_e32 v13, 0x43800000, v204
	v_mul_f32_e32 v11, 0x43800000, v205
	v_add_u32_e32 v4, v41, v32
	v_cvt_pk_fp8_f32 v195, v13, v11 op_sel:[0,0,1]
	v_add_u32_e32 v11, v41, v65
	ds_read2st64_b32 v[192:193], v11 offset0:9 offset1:10
	ds_read_b32 v4, v4
	v_add_u32_e32 v13, v42, v29
	ds_read_b32 v11, v11 offset:2816
	ds_read_b32 v13, v13
	v_add_u32_e32 v197, v42, v65
	s_waitcnt lgkmcnt(3)
	v_mul_f32_e32 v15, 0x43800000, v192
	v_mul_f32_e32 v69, 0x43800000, v193
	ds_read2st64_b32 v[192:193], v197 offset0:13 offset1:14
	s_waitcnt lgkmcnt(3)
	v_mul_f32_e32 v4, 0x43800000, v4
	v_mov_b32_e32 v196, v5
	v_cvt_pk_fp8_f32 v196, v4, v15
	s_waitcnt lgkmcnt(1)
	v_mul_f32_e32 v4, 0x43800000, v13
	ds_read_b32 v13, v197 offset:3840
	s_waitcnt lgkmcnt(1)
	v_mul_f32_e32 v15, 0x43800000, v192
	v_mov_b32_e32 v197, v5
	v_cvt_pk_fp8_f32 v197, v4, v15
	v_mul_f32_e32 v11, 0x43800000, v11
	v_cvt_pk_fp8_f32 v196, v69, v11 op_sel:[0,0,1]
	v_mul_f32_e32 v4, 0x43800000, v193
	s_waitcnt lgkmcnt(0)
	v_mul_f32_e32 v11, 0x43800000, v13
	v_cvt_pk_fp8_f32 v197, v4, v11 op_sel:[0,0,1]
	v_add_u32_e32 v4, s99, v38
	v_lshlrev_b64 v[192:193], 10, v[4:5]
	v_add_u32_e32 v4, v44, v65
	ds_read2st64_b32 v[198:199], v4 offset1:1
	ds_read2st64_b32 v[200:201], v4 offset0:2 offset1:3
	ds_read2st64_b32 v[202:203], v4 offset0:4 offset1:5
	ds_read2st64_b32 v[204:205], v4 offset0:6 offset1:7
	v_lshl_add_u64 v[192:193], v[190:191], 0, v[192:193]
	global_store_dwordx4 v[192:193], v[194:197], off
	s_waitcnt lgkmcnt(3)
	v_mul_f32_e32 v4, 0x43800000, v198
	v_mul_f32_e32 v11, 0x43800000, v199
	v_mov_b32_e32 v198, v5
	v_cvt_pk_fp8_f32 v198, v4, v11
	s_waitcnt lgkmcnt(2)
	v_mul_f32_e32 v4, 0x43800000, v200
	v_mul_f32_e32 v11, 0x43800000, v201
	v_mov_b32_e32 v199, v5
	v_cvt_pk_fp8_f32 v198, v4, v11 op_sel:[0,0,1]
	s_waitcnt lgkmcnt(1)
	v_mul_f32_e32 v4, 0x43800000, v202
	v_mul_f32_e32 v11, 0x43800000, v203
	v_cvt_pk_fp8_f32 v199, v4, v11
	s_waitcnt lgkmcnt(0)
	v_mul_f32_e32 v13, 0x43800000, v204
	v_mul_f32_e32 v11, 0x43800000, v205
	v_add_u32_e32 v4, v45, v32
	v_cvt_pk_fp8_f32 v199, v13, v11 op_sel:[0,0,1]
	v_add_u32_e32 v11, v45, v65
	ds_read2st64_b32 v[192:193], v11 offset0:9 offset1:10
	ds_read_b32 v4, v4
	v_add_u32_e32 v13, v46, v29
	ds_read_b32 v11, v11 offset:2816
	ds_read_b32 v13, v13
	v_add_u32_e32 v194, v46, v65
	s_waitcnt lgkmcnt(3)
	v_mul_f32_e32 v15, 0x43800000, v192
	v_mul_f32_e32 v69, 0x43800000, v193
	ds_read2st64_b32 v[192:193], v194 offset0:13 offset1:14
	s_waitcnt lgkmcnt(3)
	v_mul_f32_e32 v4, 0x43800000, v4
	v_mov_b32_e32 v200, v5
	v_cvt_pk_fp8_f32 v200, v4, v15
	s_waitcnt lgkmcnt(1)
	v_mul_f32_e32 v4, 0x43800000, v13
	ds_read_b32 v13, v194 offset:3840
	s_waitcnt lgkmcnt(1)
	v_mul_f32_e32 v15, 0x43800000, v192
	v_mov_b32_e32 v201, v5
	v_cvt_pk_fp8_f32 v201, v4, v15
	v_mul_f32_e32 v11, 0x43800000, v11
	v_cvt_pk_fp8_f32 v200, v69, v11 op_sel:[0,0,1]
	v_mul_f32_e32 v4, 0x43800000, v193
	s_waitcnt lgkmcnt(0)
	v_mul_f32_e32 v11, 0x43800000, v13
	v_cvt_pk_fp8_f32 v201, v4, v11 op_sel:[0,0,1]
	v_add_u32_e32 v4, s99, v43
	v_lshlrev_b64 v[192:193], 10, v[4:5]
	v_lshl_add_u64 v[190:191], v[190:191], 0, v[192:193]
	global_store_dwordx4 v[190:191], v[198:201], off
	s_waitcnt lgkmcnt(0)
	v_add_u32_e32 v4, v9, v17
	s_waitcnt vmcnt(19)
	ds_write_b128 v4, v[18:21]
	s_waitcnt vmcnt(18)
	ds_write_b128 v4, v[70:73] offset:1024
	v_add_u32_e32 v4, v9, v22
	s_waitcnt vmcnt(17)
	ds_write_b128 v4, v[74:77] offset:2048
	s_waitcnt vmcnt(16)
	ds_write_b128 v4, v[78:81] offset:3072
	v_add_u32_e32 v4, v9, v23
	s_waitcnt vmcnt(15)
	ds_write_b128 v4, v[82:85] offset:4096
	s_waitcnt vmcnt(14)
	ds_write_b128 v4, v[86:89] offset:5120
	v_add_u32_e32 v4, v9, v24
	s_waitcnt vmcnt(13)
	ds_write_b128 v4, v[90:93] offset:6144
	s_waitcnt vmcnt(12)
	ds_write_b128 v4, v[94:97] offset:7168
	v_add_u32_e32 v4, v9, v25
	s_waitcnt vmcnt(11)
	ds_write_b128 v4, v[98:101] offset:8192
	s_waitcnt vmcnt(10)
	ds_write_b128 v4, v[102:105] offset:9216
	v_add_u32_e32 v4, v9, v26
	s_waitcnt vmcnt(9)
	ds_write_b128 v4, v[106:109] offset:10240
	s_waitcnt vmcnt(8)
	ds_write_b128 v4, v[110:113] offset:11264
	v_add_u32_e32 v4, v9, v27
	s_waitcnt vmcnt(7)
	ds_write_b128 v4, v[114:117] offset:12288
	s_waitcnt vmcnt(6)
	ds_write_b128 v4, v[118:121] offset:13312
	v_add_u32_e32 v4, v9, v64
	s_waitcnt vmcnt(5)
	ds_write_b128 v4, v[122:125] offset:14336
	s_waitcnt vmcnt(4)
	ds_write_b128 v4, v[126:129] offset:15360
	s_waitcnt lgkmcnt(0)
	s_branch .Lpp_egu_chk
; #define GAS __attribute__((address_space(1)))
; __device__ __forceinline__ void p0_transpose_item64_f8(const float* W, int K, int N, unsigned char* WT, int dst_n0, LAS float* scr, int kb, int nb, int lane, const float wsc) {
;     ...
;     const int c = lane & 3;
; #pragma unroll
;     for (int j = 0; j < 4; ++j) { const int n = (lane >> 2) + 16 * j;
;         unsigned o[4];
; #pragma unroll
;         for (int d = 0; d < 4; ++d) { float f[4];
; #pragma unroll
;             for (int e = 0; e < 4; ++e) { const int k = 16 * c + 4 * d + e; f[e] = scr[k * 64 + 4 * ((n >> 2) ^ (k >> 3)) + (n & 3)] * wsc; }
;             int p = __builtin_amdgcn_cvt_pk_fp8_f32(f[0], f[1], 0, false); p = __builtin_amdgcn_cvt_pk_fp8_f32(f[2], f[3], p, true); o[d] = (unsigned)p; }
;         u32x4 ov; ov.x = o[0]; ov.y = o[1]; ov.z = o[2]; ov.w = o[3];
;         *(GAS u32x4*)(WT + (size_t)(dst_n0 + n) * K + k0 + 16 * c) = ov; }
.Lpp_egu_tail:
	v_add_u32_e32 v4, v30, v65
	ds_read2st64_b32 v[18:19], v4 offset1:1
	ds_read2st64_b32 v[20:21], v4 offset0:2 offset1:3
	ds_read2st64_b32 v[72:73], v4 offset0:4 offset1:5
	ds_read2st64_b32 v[74:75], v4 offset0:6 offset1:7
	v_mov_b32_e32 v70, v5
	v_mov_b32_e32 v71, v5
	s_waitcnt lgkmcnt(3)
	v_mul_f32_e32 v4, 0x43800000, v18
	v_mul_f32_e32 v11, 0x43800000, v19
	v_cvt_pk_fp8_f32 v70, v4, v11
	s_waitcnt lgkmcnt(2)
	v_mul_f32_e32 v4, 0x43800000, v20
	v_mul_f32_e32 v11, 0x43800000, v21
	s_waitcnt lgkmcnt(0)
	v_mul_f32_e32 v13, 0x43800000, v74
	v_cvt_pk_fp8_f32 v70, v4, v11 op_sel:[0,0,1]
	v_mul_f32_e32 v4, 0x43800000, v72
	v_mul_f32_e32 v11, 0x43800000, v73
	v_cvt_pk_fp8_f32 v71, v4, v11
	v_mul_f32_e32 v11, 0x43800000, v75
	v_add_u32_e32 v4, v31, v32
	ds_read_b32 v4, v4
	v_cvt_pk_fp8_f32 v71, v13, v11 op_sel:[0,0,1]
	v_add_u32_e32 v11, v31, v65
	ds_read2st64_b32 v[20:21], v11 offset0:9 offset1:10
	v_add_u32_e32 v13, v33, v29
	ds_read_b32 v11, v11 offset:2816
	ds_read_b32 v13, v13
	v_add_u32_e32 v73, v33, v65
	s_waitcnt lgkmcnt(2)
	v_mul_f32_e32 v15, 0x43800000, v20
	v_mul_f32_e32 v69, 0x43800000, v21
	ds_read2st64_b32 v[20:21], v73 offset0:13 offset1:14
	v_mul_f32_e32 v4, 0x43800000, v4
	v_mov_b32_e32 v72, v5
	v_cvt_pk_fp8_f32 v72, v4, v15
	s_waitcnt lgkmcnt(1)
	v_mul_f32_e32 v4, 0x43800000, v13
	ds_read_b32 v13, v73 offset:3840
	s_waitcnt lgkmcnt(1)
	v_mul_f32_e32 v15, 0x43800000, v20
	v_mov_b32_e32 v73, v5
	v_cvt_pk_fp8_f32 v73, v4, v15
	v_mul_f32_e32 v11, 0x43800000, v11
	v_cvt_pk_fp8_f32 v72, v69, v11 op_sel:[0,0,1]
	v_mul_f32_e32 v4, 0x43800000, v21
	s_waitcnt lgkmcnt(0)
	v_mul_f32_e32 v11, 0x43800000, v13
	v_cvt_pk_fp8_f32 v73, v4, v11 op_sel:[0,0,1]
	v_add_u32_e32 v4, s74, v28
	v_lshlrev_b64 v[20:21], 10, v[4:5]
	v_add_u32_e32 v4, v35, v65
	ds_read2st64_b32 v[74:75], v4 offset1:1
	ds_read2st64_b32 v[76:77], v4 offset0:2 offset1:3
	ds_read2st64_b32 v[78:79], v4 offset0:4 offset1:5
	ds_read2st64_b32 v[80:81], v4 offset0:6 offset1:7
	v_lshl_add_u64 v[18:19], s[0:1], 0, v[6:7]
	v_lshl_add_u64 v[20:21], v[18:19], 0, v[20:21]
	global_store_dwordx4 v[20:21], v[70:73], off
	s_waitcnt lgkmcnt(3)
	v_mul_f32_e32 v4, 0x43800000, v74
	v_mul_f32_e32 v11, 0x43800000, v75
	v_mov_b32_e32 v74, v5
	v_cvt_pk_fp8_f32 v74, v4, v11
	s_waitcnt lgkmcnt(2)
	v_mul_f32_e32 v4, 0x43800000, v76
	v_mul_f32_e32 v11, 0x43800000, v77
	v_mov_b32_e32 v75, v5
	v_cvt_pk_fp8_f32 v74, v4, v11 op_sel:[0,0,1]
	s_waitcnt lgkmcnt(1)
	v_mul_f32_e32 v4, 0x43800000, v78
	v_mul_f32_e32 v11, 0x43800000, v79
	v_cvt_pk_fp8_f32 v75, v4, v11
	s_waitcnt lgkmcnt(0)
	v_mul_f32_e32 v13, 0x43800000, v80
	v_mul_f32_e32 v11, 0x43800000, v81
	v_add_u32_e32 v4, v36, v32
	v_cvt_pk_fp8_f32 v75, v13, v11 op_sel:[0,0,1]
	v_add_u32_e32 v11, v36, v65
	ds_read2st64_b32 v[20:21], v11 offset0:9 offset1:10
	ds_read_b32 v4, v4
	v_add_u32_e32 v13, v37, v29
	ds_read_b32 v11, v11 offset:2816
	ds_read_b32 v13, v13
	v_add_u32_e32 v70, v37, v65
	s_waitcnt lgkmcnt(3)
	v_mul_f32_e32 v15, 0x43800000, v20
	v_mul_f32_e32 v69, 0x43800000, v21
	ds_read2st64_b32 v[20:21], v70 offset0:13 offset1:14
	s_waitcnt lgkmcnt(3)
	v_mul_f32_e32 v4, 0x43800000, v4
	v_mov_b32_e32 v76, v5
	v_cvt_pk_fp8_f32 v76, v4, v15
	s_waitcnt lgkmcnt(1)
	v_mul_f32_e32 v4, 0x43800000, v13
	ds_read_b32 v13, v70 offset:3840
	s_waitcnt lgkmcnt(1)
	v_mul_f32_e32 v15, 0x43800000, v20
	v_mov_b32_e32 v77, v5
	v_cvt_pk_fp8_f32 v77, v4, v15
	v_mul_f32_e32 v11, 0x43800000, v11
	v_cvt_pk_fp8_f32 v76, v69, v11 op_sel:[0,0,1]
	v_mul_f32_e32 v4, 0x43800000, v21
	s_waitcnt lgkmcnt(0)
	v_mul_f32_e32 v11, 0x43800000, v13
	v_cvt_pk_fp8_f32 v77, v4, v11 op_sel:[0,0,1]
	v_add_u32_e32 v4, s74, v34
	v_lshlrev_b64 v[20:21], 10, v[4:5]
	v_add_u32_e32 v4, v39, v65
	ds_read2st64_b32 v[70:71], v4 offset1:1
	ds_read2st64_b32 v[72:73], v4 offset0:2 offset1:3
	ds_read2st64_b32 v[78:79], v4 offset0:4 offset1:5
	ds_read2st64_b32 v[80:81], v4 offset0:6 offset1:7
	v_lshl_add_u64 v[20:21], v[18:19], 0, v[20:21]
	global_store_dwordx4 v[20:21], v[74:77], off
	s_waitcnt lgkmcnt(3)
; #define GAS __attribute__((address_space(1)))
; #define LDS_WAIT() asm volatile("s_waitcnt lgkmcnt(0)" ::: "memory")
; __device__ __forceinline__ void p0_transpose_item64_f8(const float* W, int K, int N, unsigned char* WT, int dst_n0, LAS float* scr, int kb, int nb, int lane, const float wsc) {
;     ...
;     const int c = lane & 3;
; #pragma unroll
;     for (int j = 0; j < 4; ++j) { const int n = (lane >> 2) + 16 * j;
;         unsigned o[4];
; #pragma unroll
;         for (int d = 0; d < 4; ++d) { float f[4];
; #pragma unroll
;             for (int e = 0; e < 4; ++e) { const int k = 16 * c + 4 * d + e; f[e] = scr[k * 64 + 4 * ((n >> 2) ^ (k >> 3)) + (n & 3)] * wsc; }
;             int p = __builtin_amdgcn_cvt_pk_fp8_f32(f[0], f[1], 0, false); p = __builtin_amdgcn_cvt_pk_fp8_f32(f[2], f[3], p, true); o[d] = (unsigned)p; }
;         u32x4 ov; ov.x = o[0]; ov.y = o[1]; ov.z = o[2]; ov.w = o[3];
;         *(GAS u32x4*)(WT + (size_t)(dst_n0 + n) * K + k0 + 16 * c) = ov; }
;     LDS_WAIT(); asm volatile("" ::: "memory");
	v_mul_f32_e32 v4, 0x43800000, v70
	v_mul_f32_e32 v11, 0x43800000, v71
	v_mov_b32_e32 v70, v5
	v_cvt_pk_fp8_f32 v70, v4, v11
	s_waitcnt lgkmcnt(2)
	v_mul_f32_e32 v4, 0x43800000, v72
	v_mul_f32_e32 v11, 0x43800000, v73
	v_mov_b32_e32 v71, v5
	v_cvt_pk_fp8_f32 v70, v4, v11 op_sel:[0,0,1]
	s_waitcnt lgkmcnt(1)
	v_mul_f32_e32 v4, 0x43800000, v78
	v_mul_f32_e32 v11, 0x43800000, v79
	v_cvt_pk_fp8_f32 v71, v4, v11
	s_waitcnt lgkmcnt(0)
	v_mul_f32_e32 v13, 0x43800000, v80
	v_mul_f32_e32 v11, 0x43800000, v81
	v_add_u32_e32 v4, v41, v32
	v_cvt_pk_fp8_f32 v71, v13, v11 op_sel:[0,0,1]
	v_add_u32_e32 v11, v41, v65
	ds_read2st64_b32 v[20:21], v11 offset0:9 offset1:10
	ds_read_b32 v4, v4
	v_add_u32_e32 v13, v42, v29
	ds_read_b32 v11, v11 offset:2816
	ds_read_b32 v13, v13
	v_add_u32_e32 v73, v42, v65
	s_waitcnt lgkmcnt(3)
	v_mul_f32_e32 v15, 0x43800000, v20
	v_mul_f32_e32 v69, 0x43800000, v21
	ds_read2st64_b32 v[20:21], v73 offset0:13 offset1:14
	s_waitcnt lgkmcnt(3)
	v_mul_f32_e32 v4, 0x43800000, v4
	v_mov_b32_e32 v72, v5
	v_cvt_pk_fp8_f32 v72, v4, v15
	s_waitcnt lgkmcnt(1)
	v_mul_f32_e32 v4, 0x43800000, v13
	ds_read_b32 v13, v73 offset:3840
	s_waitcnt lgkmcnt(1)
	v_mul_f32_e32 v15, 0x43800000, v20
	v_mov_b32_e32 v73, v5
	v_cvt_pk_fp8_f32 v73, v4, v15
	v_mul_f32_e32 v11, 0x43800000, v11
	v_cvt_pk_fp8_f32 v72, v69, v11 op_sel:[0,0,1]
	v_mul_f32_e32 v4, 0x43800000, v21
	s_waitcnt lgkmcnt(0)
	v_mul_f32_e32 v11, 0x43800000, v13
	v_cvt_pk_fp8_f32 v73, v4, v11 op_sel:[0,0,1]
	v_add_u32_e32 v4, s74, v38
	v_lshlrev_b64 v[20:21], 10, v[4:5]
	v_add_u32_e32 v4, v44, v65
	ds_read2st64_b32 v[74:75], v4 offset1:1
	ds_read2st64_b32 v[76:77], v4 offset0:2 offset1:3
	ds_read2st64_b32 v[78:79], v4 offset0:4 offset1:5
	ds_read2st64_b32 v[80:81], v4 offset0:6 offset1:7
	v_lshl_add_u64 v[20:21], v[18:19], 0, v[20:21]
	global_store_dwordx4 v[20:21], v[70:73], off
	s_waitcnt lgkmcnt(3)
	v_mul_f32_e32 v4, 0x43800000, v74
	v_mul_f32_e32 v11, 0x43800000, v75
	v_mov_b32_e32 v74, v5
	v_cvt_pk_fp8_f32 v74, v4, v11
	s_waitcnt lgkmcnt(2)
	v_mul_f32_e32 v4, 0x43800000, v76
	v_mul_f32_e32 v11, 0x43800000, v77
	v_mov_b32_e32 v75, v5
	v_cvt_pk_fp8_f32 v74, v4, v11 op_sel:[0,0,1]
	s_waitcnt lgkmcnt(1)
	v_mul_f32_e32 v4, 0x43800000, v78
	v_mul_f32_e32 v11, 0x43800000, v79
	v_cvt_pk_fp8_f32 v75, v4, v11
	s_waitcnt lgkmcnt(0)
	v_mul_f32_e32 v13, 0x43800000, v80
	v_mul_f32_e32 v11, 0x43800000, v81
	v_add_u32_e32 v4, v45, v32
	v_cvt_pk_fp8_f32 v75, v13, v11 op_sel:[0,0,1]
	v_add_u32_e32 v11, v45, v65
	ds_read2st64_b32 v[20:21], v11 offset0:9 offset1:10
	ds_read_b32 v4, v4
	v_add_u32_e32 v13, v46, v29
	ds_read_b32 v11, v11 offset:2816
	ds_read_b32 v13, v13
	v_add_u32_e32 v70, v46, v65
	s_waitcnt lgkmcnt(3)
	v_mul_f32_e32 v15, 0x43800000, v20
	v_mul_f32_e32 v69, 0x43800000, v21
	ds_read2st64_b32 v[20:21], v70 offset0:13 offset1:14
	s_waitcnt lgkmcnt(3)
	v_mul_f32_e32 v4, 0x43800000, v4
	v_mov_b32_e32 v76, v5
	v_cvt_pk_fp8_f32 v76, v4, v15
	s_waitcnt lgkmcnt(1)
	v_mul_f32_e32 v4, 0x43800000, v13
	ds_read_b32 v13, v70 offset:3840
	s_waitcnt lgkmcnt(1)
	v_mul_f32_e32 v15, 0x43800000, v20
	v_mov_b32_e32 v77, v5
	v_cvt_pk_fp8_f32 v77, v4, v15
	v_mul_f32_e32 v11, 0x43800000, v11
	v_cvt_pk_fp8_f32 v76, v69, v11 op_sel:[0,0,1]
	v_mul_f32_e32 v4, 0x43800000, v21
	s_waitcnt lgkmcnt(0)
	v_mul_f32_e32 v11, 0x43800000, v13
	v_cvt_pk_fp8_f32 v77, v4, v11 op_sel:[0,0,1]
	v_add_u32_e32 v4, s74, v43
	v_lshlrev_b64 v[20:21], 10, v[4:5]
	v_lshl_add_u64 v[18:19], v[18:19], 0, v[20:21]
	global_store_dwordx4 v[18:19], v[74:77], off
	s_waitcnt lgkmcnt(0)
